# speedup vs baseline: 1.0342x; 1.0058x over previous
_Z11proj_kernelPKfS0_S0_PKDF16_S0_S0_S0_PDF16_S3_S3_Pj:
	s_ashr_i32 s12, s2, 6
	s_load_dwordx8 s[4:11], s[0:1], 0x0
	s_cmp_gt_u32 s2, 63
	s_cselect_b64 s[22:23], -1, 0
	s_cmp_lg_u32 s12, 1
	s_cselect_b64 s[18:19], -1, 0
	s_cmp_eq_u32 s12, 1
	s_cselect_b64 s[20:21], -1, 0
	s_and_b64 s[14:15], s[20:21], exec
	s_waitcnt lgkmcnt(0)
	s_cselect_b32 s14, s6, s8
	s_cselect_b32 s15, s7, s9
	s_ashr_i32 s13, s12, 31
	s_lshl_b32 s28, s2, 7
	s_lshl_b64 s[6:7], s[12:13], 19
	s_and_b32 s3, s28, 0x1f80
	s_cmp_lt_u32 s2, 64
	s_cselect_b64 vcc, -1, 0
	v_lshrrev_b32_e32 v1, 2, v0
	v_lshrrev_b32_e32 v2, 2, v0
	v_and_b32_e32 v2, 0x70, v2
	v_bfe_u32 v254, v0, 3, 3
	v_or_b32_e32 v254, v2, v254
	v_or_b32_e32 v2, s3, v254
	s_and_b64 s[8:9], vcc, exec
	s_cselect_b32 s25, s5, s15
	s_cselect_b32 s24, s4, s14
	v_lshlrev_b32_e32 v2, 11, v2
	v_mov_b32_e32 v3, 0
	v_lshlrev_b32_e32 v6, 4, v0
	s_add_u32 s4, s10, s6
	v_lshl_add_u64 v[4:5], s[24:25], 0, v[2:3]
	v_and_b32_e32 v6, 0x70, v6
	v_mov_b32_e32 v7, v3
	v_lshlrev_b32_e32 v56, 4, v0
	v_mov_b32_e32 v57, v3
	s_addc_u32 s5, s11, s7
	v_lshl_add_u64 v[4:5], v[4:5], 0, v[6:7]
	s_mov_b64 s[46:47], 0x4000
	v_lshl_add_u64 v[250:251], v[4:5], 0, s[46:47]
	s_movk_i32 s8, 0x2000
	v_lshl_add_u64 v[6:7], s[4:5], 0, v[56:57]
	global_load_dwordx4 v[8:11], v[4:5], off sc1 nt
	global_load_dwordx4 v[12:15], v[250:251], off sc1 nt
	global_load_dwordx4 v[16:19], v56, s[4:5] sc1
	v_add_co_u32_e64 v28, s[4:5], s8, v6
	s_mov_b32 s33, 0xa000
	s_nop 0
	v_addc_co_u32_e64 v29, s[4:5], 0, v7, s[4:5]
	s_movk_i32 s4, 0x4000
	s_nop 0
	v_add_co_u32_e64 v30, s[4:5], s4, v6
	s_mov_b32 s6, 0xe000
	s_nop 0
	v_addc_co_u32_e64 v31, s[4:5], 0, v7, s[4:5]
	global_load_dwordx4 v[20:23], v[28:29], off sc1
	global_load_dwordx4 v[24:27], v[30:31], off sc1
	s_movk_i32 s4, 0x6000
	v_add_co_u32_e64 v40, s[4:5], s4, v6
	v_lshlrev_b32_e32 v57, 6, v1
	s_nop 0
	v_addc_co_u32_e64 v41, s[4:5], 0, v7, s[4:5]
	global_load_dwordx4 v[28:31], v[40:41], off sc1
	global_load_dwordx4 v[32:35], v[4:5], off offset:128 sc1 nt
	global_load_dwordx4 v[36:39], v[250:251], off offset:128 sc1 nt
	s_mov_b32 s4, 0x8000
	v_add_co_u32_e64 v40, s[4:5], s4, v6
	v_bitop3_b32 v58, v56, 48, v0 bitop3:0x48
	s_nop 0
	v_addc_co_u32_e64 v41, s[4:5], 0, v7, s[4:5]
	v_add_co_u32_e64 v44, s[4:5], s33, v6
	global_load_dwordx4 v[40:43], v[40:41], off sc1
	s_nop 0
	v_addc_co_u32_e64 v45, s[4:5], 0, v7, s[4:5]
	s_mov_b32 s4, 0xc000
	s_nop 0
	v_add_co_u32_e64 v48, s[4:5], s4, v6
	global_load_dwordx4 v[44:47], v[44:45], off sc1
	s_nop 0
	v_addc_co_u32_e64 v49, s[4:5], 0, v7, s[4:5]
	v_add_co_u32_e64 v52, s[4:5], s6, v6
	global_load_dwordx4 v[48:51], v[48:49], off sc1
	s_nop 0
	v_addc_co_u32_e64 v53, s[4:5], 0, v7, s[4:5]
	global_load_dwordx4 v[52:55], v[52:53], off sc1
	s_mov_b32 s4, 0x1e000
	v_bfe_u32 v57, v0, 1, 2
	v_bfe_u32 v58, v254, 2, 2
	v_xor_b32_e32 v57, v57, v58
	v_lshlrev_b32_e32 v57, 4, v57
	v_and_b32_e32 v58, 1, v0
	v_lshl_or_b32 v57, v58, 3, v57
	v_lshl_add_u32 v209, v254, 6, v57
	v_xor_b32_e32 v248, 32, v209
	v_add_u32_e32 v248, 0x200, v248
	v_add_u32_e32 v208, 0, v56
	v_readfirstlane_b32 s30, v0
	v_bfe_u32 v207, v0, 5, 1
	v_bitop3_b32 v1, v207, v1, 3 bitop3:0x78
	v_lshlrev_b32_e32 v210, 4, v1
	s_mov_b32 s34, 0x14000
	v_add_u32_e32 v213, 0x2000, v208
	s_mov_b32 s43, 0
	s_lshr_b32 s29, s30, 6
	s_mov_b32 s35, -2
	s_mov_b32 s36, 0xffff2000
	s_mov_b32 s37, 0xffff4000
	s_mov_b32 s38, 0xffff6000
	s_movk_i32 s39, 0x8000
	s_movk_i32 s40, 0xa000
	s_movk_i32 s41, 0xc000
	s_movk_i32 s42, 0xe000
	s_mov_b64 s[26:27], 0x100
	v_mov_b32_e32 v56, v3
	v_mov_b32_e32 v57, v3
	v_mov_b32_e32 v58, v3
	v_mov_b32_e32 v59, v3
	v_mov_b32_e32 v60, v3
	v_mov_b32_e32 v61, v3
	v_mov_b32_e32 v62, v3
	v_mov_b32_e32 v63, v3
	v_mov_b32_e32 v64, v3
	v_mov_b32_e32 v65, v3
	v_mov_b32_e32 v66, v3
	v_mov_b32_e32 v67, v3
	v_mov_b32_e32 v68, v3
	v_mov_b32_e32 v69, v3
	v_mov_b32_e32 v70, v3
	s_waitcnt vmcnt(11)
	v_cvt_pk_f16_f32 v8, v8, v9
	v_cvt_pk_f16_f32 v9, v10, v11
	s_waitcnt vmcnt(10)
	v_cvt_pk_f16_f32 v10, v12, v13
	v_cvt_pk_f16_f32 v11, v14, v15
	ds_write_b64 v209, v[8:9]
	ds_write_b64 v248, v[10:11]
	v_and_b32_e32 v10, 31, v0
	s_waitcnt vmcnt(9)
	ds_write_b128 v208, v[16:19] offset:8192
	s_waitcnt vmcnt(8)
	ds_write_b128 v208, v[20:23] offset:16384
	s_waitcnt vmcnt(7)
	ds_write_b128 v208, v[24:27] offset:24576
	s_load_dwordx2 s[16:17], s[0:1], 0x50
	s_load_dwordx4 s[12:15], s[0:1], 0x40
	s_load_dwordx8 s[4:11], s[0:1], 0x20
	s_lshl_b32 s0, s30, 1
	s_and_b32 s31, s0, 0x180
	s_lshr_b32 s0, s30, 2
	v_bfe_u32 v11, v0, 2, 2
	s_and_b32 s0, s0, 0x3fffffc0
	s_waitcnt vmcnt(5)
	v_cvt_pk_f16_f32 v8, v32, v33
	v_cvt_pk_f16_f32 v9, v34, v35
	v_or_b32_e32 v12, s31, v10
	v_or_b32_e32 v206, s0, v10
	v_bitop3_b32 v1, v207, v11, 2 bitop3:0x36
	s_waitcnt vmcnt(4)
	v_cvt_pk_f16_f32 v10, v36, v37
	v_cvt_pk_f16_f32 v11, v38, v39
	s_mov_b32 s0, 0x10000
	ds_write_b128 v208, v[28:31] offset:32768
	ds_write_b64 v209, v[8:9] offset:40960
	ds_write_b64 v248, v[10:11] offset:40960
	v_add_co_u32_e64 v8, s[0:1], s0, v6
	global_load_dwordx4 v[154:157], v[250:251], off offset:256 sc1 nt
	global_load_dwordx4 v[162:165], v[4:5], off offset:256 sc1 nt
	v_addc_co_u32_e64 v9, s[0:1], 0, v7, s[0:1]
	s_mov_b32 s0, 0x12000
	global_load_dwordx4 v[158:161], v[8:9], off sc1
	v_add_co_u32_e64 v8, s[0:1], s0, v6
	v_lshl_add_u32 v211, v12, 6, 0
	s_nop 0
	v_addc_co_u32_e64 v9, s[0:1], 0, v7, s[0:1]
	v_add_co_u32_e64 v10, s[0:1], s34, v6
	v_add_u32_e32 v14, 0x12000, v208
	s_nop 0
	v_addc_co_u32_e64 v11, s[0:1], 0, v7, s[0:1]
	s_mov_b32 s0, 0x16000
	s_nop 0
	v_add_co_u32_e64 v12, s[0:1], s0, v6
	s_waitcnt vmcnt(3)
	ds_write_b128 v14, v[52:55]
	v_addc_co_u32_e64 v13, s[0:1], 0, v7, s[0:1]
	s_mov_b32 s0, 0x18000
	s_nop 0
	v_add_co_u32_e64 v14, s[0:1], s0, v6
	ds_write_b128 v208, v[40:43] offset:49152
	s_nop 0
	v_addc_co_u32_e64 v15, s[0:1], 0, v7, s[0:1]
	s_mov_b32 s0, 0x1a000
	s_nop 0
	v_add_co_u32_e64 v16, s[0:1], s0, v6
	ds_write_b128 v208, v[44:47] offset:57344
	s_nop 0
	v_addc_co_u32_e64 v17, s[0:1], 0, v7, s[0:1]
	s_mov_b32 s0, 0x1c000
	ds_write_b128 v213, v[48:51] offset:57344
	v_add_co_u32_e64 v18, s[0:1], s0, v6
	v_add_u32_e32 v216, v211, v210
	s_nop 0
	v_addc_co_u32_e64 v19, s[0:1], 0, v7, s[0:1]
	global_load_dwordx4 v[174:177], v[8:9], off sc1
	global_load_dwordx4 v[166:169], v[10:11], off sc1
	global_load_dwordx4 v[170:173], v[12:13], off sc1
	global_load_dwordx4 v[142:145], v[250:251], off offset:384 sc1 nt
	global_load_dwordx4 v[150:153], v[4:5], off offset:384 sc1 nt
	global_load_dwordx4 v[138:141], v[14:15], off sc1
	global_load_dwordx4 v[146:149], v[16:17], off sc1
	global_load_dwordx4 v[134:137], v[18:19], off sc1
	s_mov_b32 s0, 0x1e000
	v_add_co_u32_e64 v8, s[0:1], s0, v6
	s_nop 1
	v_addc_co_u32_e64 v9, s[0:1], 0, v7, s[0:1]
	global_load_dwordx4 v[130:133], v[8:9], off sc1
	s_waitcnt lgkmcnt(0)
	s_barrier
	v_lshl_add_u32 v218, v206, 6, 0
	v_add_u32_e32 v217, v218, v210
	ds_read_b128 v[198:201], v216 offset:8192
	ds_read_b128 v[194:197], v216 offset:10240
	ds_read_b128 v[190:193], v216 offset:12288
	ds_read_b128 v[178:181], v216 offset:14336
	ds_read_b128 v[186:189], v217
	ds_read_b128 v[182:185], v217 offset:2048
	v_and_b32_e32 v20, 7, v0
	v_lshl_or_b32 v2, v20, 4, v2
	s_mov_b64 s[0:1], 0x2e000
	v_lshlrev_b32_e32 v212, 4, v1
	v_lshl_add_u64 v[202:203], v[6:7], 0, s[0:1]
	s_mov_b64 s[0:1], 0x290
	v_lshl_add_u64 v[4:5], s[24:25], 0, v[2:3]
	v_lshl_add_u64 v[204:205], v[4:5], 0, s[0:1]
	v_lshl_add_u64 v[252:253], v[204:205], 0, s[46:47]
	s_mov_b64 s[24:25], 0x10000
	v_mov_b32_e32 v2, v3
	v_mov_b32_e32 v4, v3
	v_mov_b32_e32 v5, v3
	v_mov_b32_e32 v6, v3
	v_mov_b32_e32 v7, v3
	v_mov_b32_e32 v8, v3
	v_mov_b32_e32 v9, v3
	v_mov_b32_e32 v10, v3
	v_mov_b32_e32 v11, v3
	v_mov_b32_e32 v12, v3
	v_mov_b32_e32 v13, v3
	v_mov_b32_e32 v14, v3
	v_mov_b32_e32 v15, v3
	v_mov_b32_e32 v16, v3
	v_mov_b32_e32 v17, v3
	v_mov_b32_e32 v18, v3
	v_mov_b32_e32 v19, v3
	v_mov_b32_e32 v20, v3
	v_mov_b32_e32 v21, v3
	v_mov_b32_e32 v22, v3
	v_mov_b32_e32 v23, v3
	v_mov_b32_e32 v24, v3
	v_mov_b32_e32 v25, v3
	v_mov_b32_e32 v26, v3
	v_mov_b32_e32 v27, v3
	v_mov_b32_e32 v28, v3
	v_mov_b32_e32 v29, v3
	v_mov_b32_e32 v30, v3
	v_mov_b32_e32 v31, v3
	v_mov_b32_e32 v32, v3
	v_mov_b32_e32 v33, v3
	v_mov_b32_e32 v34, v3
	v_mov_b32_e32 v35, v3
	v_mov_b32_e32 v36, v3
	v_mov_b32_e32 v37, v3
	v_mov_b32_e32 v38, v3
	v_mov_b32_e32 v39, v3
	v_mov_b32_e32 v40, v3
	v_mov_b32_e32 v41, v3
	v_mov_b32_e32 v42, v3
	v_mov_b32_e32 v43, v3
	v_mov_b32_e32 v44, v3
	v_mov_b32_e32 v45, v3
	v_mov_b32_e32 v46, v3
	v_mov_b32_e32 v47, v3
	v_mov_b32_e32 v48, v3
	v_mov_b32_e32 v49, v3
	v_mov_b32_e32 v50, v3
	v_mov_b32_e32 v51, v3
	v_mov_b32_e32 v52, v3
	v_mov_b32_e32 v53, v3
	v_mov_b32_e32 v54, v3
	v_mov_b32_e32 v55, v3
	v_mov_b32_e32 v71, v3
	v_mov_b32_e32 v72, v3
	v_mov_b32_e32 v73, v3
	v_mov_b32_e32 v74, v3
	v_mov_b32_e32 v75, v3
	v_mov_b32_e32 v76, v3
	v_mov_b32_e32 v77, v3
	v_mov_b32_e32 v78, v3
	v_mov_b32_e32 v79, v3
	v_mov_b32_e32 v80, v3
	v_mov_b32_e32 v81, v3
	v_mov_b32_e32 v82, v3
	v_mov_b32_e32 v83, v3
	v_mov_b32_e32 v84, v3
	v_mov_b32_e32 v85, v3
	v_mov_b32_e32 v86, v3
	v_mov_b32_e32 v87, v3
	v_mov_b32_e32 v88, v3
	v_mov_b32_e32 v89, v3
	v_mov_b32_e32 v90, v3
	v_mov_b32_e32 v91, v3
	v_mov_b32_e32 v92, v3
	v_mov_b32_e32 v93, v3
	v_mov_b32_e32 v94, v3
	v_mov_b32_e32 v95, v3
	v_mov_b32_e32 v96, v3
	v_mov_b32_e32 v97, v3
	v_mov_b32_e32 v98, v3
	v_mov_b32_e32 v99, v3
	v_mov_b32_e32 v100, v3
	v_mov_b32_e32 v101, v3
	v_mov_b32_e32 v102, v3
	v_mov_b32_e32 v103, v3
	v_mov_b32_e32 v104, v3
	v_mov_b32_e32 v105, v3
	v_mov_b32_e32 v106, v3
	v_mov_b32_e32 v107, v3
	v_mov_b32_e32 v108, v3
	v_mov_b32_e32 v109, v3
	v_mov_b32_e32 v110, v3
	v_mov_b32_e32 v111, v3
	v_mov_b32_e32 v112, v3
	v_mov_b32_e32 v113, v3
	v_mov_b32_e32 v114, v3
	v_mov_b32_e32 v115, v3
	v_mov_b32_e32 v116, v3
	v_mov_b32_e32 v117, v3
	v_mov_b32_e32 v118, v3
	v_mov_b32_e32 v119, v3
	v_mov_b32_e32 v120, v3
	v_mov_b32_e32 v121, v3
	v_mov_b32_e32 v122, v3
	v_mov_b32_e32 v123, v3
	v_mov_b32_e32 v124, v3
	v_mov_b32_e32 v125, v3
	v_mov_b32_e32 v126, v3
	v_mov_b32_e32 v127, v3
	v_mov_b32_e32 v128, v3
	v_mov_b32_e32 v129, v3
	v_and_b32_e32 v1, 63, v0
	v_add_u32_e32 v215, v211, v212
	v_add_u32_e32 v214, v218, v212
.LBB1_1:
	s_waitcnt lgkmcnt(0)
	v_mfma_f32_32x32x16_f16 v[114:129], v[198:201], v[186:189], v[114:129]
	s_mov_b32 s44, s33
	s_mov_b32 s33, s43
	v_mfma_f32_32x32x16_f16 v[98:113], v[198:201], v[182:185], v[98:113]
	v_add_u32_e32 v219, s33, v215
	ds_read_b128 v[198:201], v219 offset:8192
	ds_read_b128 v[220:223], v219 offset:10240
	ds_read_b128 v[224:227], v219 offset:12288
	ds_read_b128 v[228:231], v219 offset:14336
	v_add_u32_e32 v219, s33, v214
	ds_read_b128 v[232:235], v219
	ds_read_b128 v[236:239], v219 offset:2048
	s_waitcnt vmcnt(10)
	v_cvt_pk_f16_f32 v162, v162, v163
	v_cvt_pk_f16_f32 v163, v164, v165
	v_cvt_pk_f16_f32 v164, v154, v155
	v_cvt_pk_f16_f32 v165, v156, v157
	v_add_u32_e32 v154, s34, v209
	ds_write_b64 v154, v[162:163]
	v_add_u32_e32 v154, s34, v248
	ds_write_b64 v154, v[164:165]
	v_mfma_f32_32x32x16_f16 v[82:97], v[194:197], v[186:189], v[82:97]
	v_add_u32_e32 v154, s34, v208
	s_waitcnt vmcnt(9)
	ds_write_b128 v154, v[158:161] offset:8192
	s_waitcnt vmcnt(8)
	ds_write_b128 v154, v[174:177] offset:16384
	v_mfma_f32_32x32x16_f16 v[66:81], v[194:197], v[182:185], v[66:81]
	v_mfma_f32_32x32x16_f16 v[50:65], v[190:193], v[186:189], v[50:65]
	s_waitcnt vmcnt(7)
	ds_write_b128 v154, v[166:169] offset:24576
	s_waitcnt vmcnt(6)
	ds_write_b128 v154, v[170:173] offset:32768
	v_mfma_f32_32x32x16_f16 v[34:49], v[190:193], v[182:185], v[34:49]
	v_add_co_u32_e64 v158, s[0:1], s36, v202
	global_load_dwordx4 v[154:157], v[252:253], off offset:-144 sc1 nt
	global_load_dwordx4 v[162:165], v[204:205], off offset:-144 sc1 nt
	v_addc_co_u32_e64 v159, s[0:1], -1, v203, s[0:1]
	v_add_co_u32_e64 v166, s[0:1], s37, v202
	v_mfma_f32_32x32x16_f16 v[18:33], v[178:181], v[186:189], v[18:33]
	s_nop 0
	v_addc_co_u32_e64 v167, s[0:1], -1, v203, s[0:1]
	global_load_dwordx4 v[158:161], v[158:159], off sc1
	s_nop 0
	global_load_dwordx4 v[174:177], v[166:167], off sc1
	v_add_co_u32_e64 v166, s[0:1], s38, v202
	s_nop 1
	v_addc_co_u32_e64 v167, s[0:1], -1, v203, s[0:1]
	v_add_co_u32_e64 v170, s[0:1], s39, v202
	v_mfma_f32_32x32x16_f16 v[2:17], v[178:181], v[182:185], v[2:17]
	s_nop 0
	v_addc_co_u32_e64 v171, s[0:1], -1, v203, s[0:1]
	global_load_dwordx4 v[166:169], v[166:167], off sc1
	s_nop 0
	global_load_dwordx4 v[170:173], v[170:171], off sc1
	v_add_u32_e32 v190, s44, v216
	ds_read_b128 v[178:181], v190 offset:8192
	ds_read_b128 v[182:185], v190 offset:10240
	ds_read_b128 v[186:189], v190 offset:12288
	ds_read_b128 v[190:193], v190 offset:14336
	v_add_u32_e32 v219, s44, v217
	ds_read_b128 v[194:197], v219
	ds_read_b128 v[240:243], v219 offset:2048
	s_waitcnt lgkmcnt(12)
	v_mfma_f32_32x32x16_f16 v[114:129], v[198:201], v[232:235], v[114:129]
	s_waitcnt lgkmcnt(11)
	v_mfma_f32_32x32x16_f16 v[98:113], v[198:201], v[236:239], v[98:113]
	v_mfma_f32_32x32x16_f16 v[82:97], v[220:223], v[232:235], v[82:97]
	v_mfma_f32_32x32x16_f16 v[66:81], v[220:223], v[236:239], v[66:81]
	v_mfma_f32_32x32x16_f16 v[50:65], v[224:227], v[232:235], v[50:65]
	v_mfma_f32_32x32x16_f16 v[34:49], v[224:227], v[236:239], v[34:49]
	v_mfma_f32_32x32x16_f16 v[18:33], v[228:231], v[232:235], v[18:33]
	v_mfma_f32_32x32x16_f16 v[2:17], v[228:231], v[236:239], v[2:17]
	s_waitcnt lgkmcnt(1)
	v_mfma_f32_32x32x16_f16 v[114:129], v[178:181], v[194:197], v[114:129]
	s_waitcnt lgkmcnt(0)
	s_barrier
	s_waitcnt lgkmcnt(0)
	v_mfma_f32_32x32x16_f16 v[98:113], v[178:181], v[240:243], v[98:113]
	v_add_u32_e32 v178, s44, v215
	ds_read_b128 v[220:223], v178 offset:8192
	ds_read_b128 v[224:227], v178 offset:10240
	ds_read_b128 v[228:231], v178 offset:12288
	ds_read_b128 v[232:235], v178 offset:14336
	v_add_u32_e32 v178, s44, v214
	ds_read_b128 v[236:239], v178
	ds_read_b128 v[244:247], v178 offset:2048
	s_waitcnt vmcnt(10)
	v_cvt_pk_f16_f32 v150, v150, v151
	v_cvt_pk_f16_f32 v151, v152, v153
	v_cvt_pk_f16_f32 v152, v142, v143
	v_cvt_pk_f16_f32 v153, v144, v145
	v_add_u32_e32 v142, s33, v209
	ds_write_b64 v142, v[150:151]
	v_add_u32_e32 v142, s33, v248
	ds_write_b64 v142, v[152:153]
	v_mfma_f32_32x32x16_f16 v[82:97], v[182:185], v[194:197], v[82:97]
	v_add_u32_e32 v142, s33, v208
	s_waitcnt vmcnt(9)
	ds_write_b128 v142, v[138:141] offset:8192
	s_waitcnt vmcnt(8)
	ds_write_b128 v142, v[146:149] offset:16384
	v_mfma_f32_32x32x16_f16 v[66:81], v[182:185], v[240:243], v[66:81]
	v_mfma_f32_32x32x16_f16 v[50:65], v[186:189], v[194:197], v[50:65]
	s_waitcnt vmcnt(7)
	ds_write_b128 v142, v[134:137] offset:24576
	s_waitcnt vmcnt(6)
	ds_write_b128 v142, v[130:133] offset:32768
	v_mfma_f32_32x32x16_f16 v[34:49], v[186:189], v[240:243], v[34:49]
	v_add_co_u32_e64 v130, s[0:1], s40, v202
	global_load_dwordx4 v[142:145], v[252:253], off offset:-16 sc1 nt
	global_load_dwordx4 v[150:153], v[204:205], off offset:-16 sc1 nt
	v_addc_co_u32_e64 v131, s[0:1], -1, v203, s[0:1]
	v_add_co_u32_e64 v132, s[0:1], s41, v202
	v_mfma_f32_32x32x16_f16 v[18:33], v[190:193], v[194:197], v[18:33]
	s_nop 0
	v_addc_co_u32_e64 v133, s[0:1], -1, v203, s[0:1]
	global_load_dwordx4 v[138:141], v[130:131], off sc1
	global_load_dwordx4 v[146:149], v[132:133], off sc1
	v_add_co_u32_e64 v130, s[0:1], s42, v202
	s_nop 1
	v_addc_co_u32_e64 v131, s[0:1], -1, v203, s[0:1]
	global_load_dwordx4 v[134:137], v[130:131], off sc1
	s_nop 0
	global_load_dwordx4 v[130:133], v[202:203], off sc1
	v_mfma_f32_32x32x16_f16 v[2:17], v[190:193], v[240:243], v[2:17]
	v_add_u32_e32 v178, s34, v216
	ds_read_b128 v[198:201], v178 offset:8192
	ds_read_b128 v[194:197], v178 offset:10240
	ds_read_b128 v[190:193], v178 offset:12288
	ds_read_b128 v[178:181], v178 offset:14336
	v_add_u32_e32 v182, s34, v217
	ds_read_b128 v[186:189], v182
	ds_read_b128 v[182:185], v182 offset:2048
	s_waitcnt lgkmcnt(12)
	v_mfma_f32_32x32x16_f16 v[114:129], v[220:223], v[236:239], v[114:129]
	s_waitcnt lgkmcnt(11)
	v_mfma_f32_32x32x16_f16 v[98:113], v[220:223], v[244:247], v[98:113]
	v_mfma_f32_32x32x16_f16 v[82:97], v[224:227], v[236:239], v[82:97]
	v_mfma_f32_32x32x16_f16 v[66:81], v[224:227], v[244:247], v[66:81]
	v_mfma_f32_32x32x16_f16 v[50:65], v[228:231], v[236:239], v[50:65]
	v_mfma_f32_32x32x16_f16 v[34:49], v[228:231], v[244:247], v[34:49]
	v_mfma_f32_32x32x16_f16 v[18:33], v[232:235], v[236:239], v[18:33]
	v_mfma_f32_32x32x16_f16 v[2:17], v[232:235], v[244:247], v[2:17]
	s_waitcnt lgkmcnt(0)
	s_barrier
	s_add_i32 s35, s35, 2
	v_lshl_add_u64 v[202:203], v[202:203], 0, s[24:25]
	v_lshl_add_u64 v[204:205], v[204:205], 0, s[26:27]
	v_lshl_add_u64 v[252:253], v[252:253], 0, s[26:27]
	s_mov_b32 s43, s34
	s_cmp_gt_u32 s35, 9
	s_mov_b32 s34, s44
	s_cbranch_scc0 .LBB1_1
	s_and_b64 s[0:1], s[20:21], exec
	s_cselect_b32 s6, s6, s8
	s_cselect_b32 s7, s7, s9
	s_and_b64 s[0:1], vcc, exec
	s_cselect_b32 s1, s5, s7
	s_cselect_b32 s0, s4, s6
	v_mov_b32_e32 v202, 0x3e38aa3b
	s_waitcnt lgkmcnt(1)
	v_mfma_f32_32x32x16_f16 v[114:129], v[198:201], v[186:189], v[114:129]
	v_cndmask_b32_e32 v202, 1.0, v202, vcc
	s_waitcnt lgkmcnt(0)
	v_mfma_f32_32x32x16_f16 v[98:113], v[198:201], v[182:185], v[98:113]
	ds_read_b128 v[198:201], v215 offset:8192
	ds_read_b128 v[220:223], v215 offset:10240
	ds_read_b128 v[224:227], v215 offset:12288
	ds_read_b128 v[228:231], v215 offset:14336
	ds_read_b128 v[232:235], v214
	ds_read_b128 v[236:239], v214 offset:2048
	s_waitcnt vmcnt(10)
	v_cvt_pk_f16_f32 v162, v162, v163
	v_cvt_pk_f16_f32 v163, v164, v165
	v_cvt_pk_f16_f32 v164, v154, v155
	v_cvt_pk_f16_f32 v165, v156, v157
	v_add_u32_e32 v154, 0x14000, v209
	ds_write_b64 v154, v[162:163]
	v_add_u32_e32 v154, 0x14000, v248
	ds_write_b64 v154, v[164:165]
	v_add_u32_e32 v154, 0x14000, v213
	s_waitcnt vmcnt(9)
	ds_write_b128 v154, v[158:161]
	v_add_u32_e32 v154, 0x16000, v213
	v_mfma_f32_32x32x16_f16 v[82:97], v[194:197], v[186:189], v[82:97]
	s_waitcnt vmcnt(8)
	ds_write_b128 v154, v[174:177]
	v_mfma_f32_32x32x16_f16 v[66:81], v[194:197], v[182:185], v[66:81]
	v_add_u32_e32 v154, 0x18000, v213
	s_waitcnt vmcnt(7)
	ds_write_b128 v154, v[166:169]
	v_add_u32_e32 v154, 0x1a000, v213
	v_mfma_f32_32x32x16_f16 v[50:65], v[190:193], v[186:189], v[50:65]
	s_waitcnt vmcnt(6)
	ds_write_b128 v154, v[170:173]
	v_mfma_f32_32x32x16_f16 v[34:49], v[190:193], v[182:185], v[34:49]
	v_mfma_f32_32x32x16_f16 v[18:33], v[178:181], v[186:189], v[18:33]
	v_mfma_f32_32x32x16_f16 v[2:17], v[178:181], v[182:185], v[2:17]
	ds_read_b128 v[154:157], v216 offset:49152
	ds_read_b128 v[158:161], v216 offset:51200
	ds_read_b128 v[162:165], v216 offset:53248
	ds_read_b128 v[166:169], v216 offset:55296
	ds_read_b128 v[170:173], v217 offset:40960
	ds_read_b128 v[174:177], v217 offset:43008
	s_waitcnt lgkmcnt(12)
	v_mfma_f32_32x32x16_f16 v[114:129], v[198:201], v[232:235], v[114:129]
	s_waitcnt lgkmcnt(11)
	v_mfma_f32_32x32x16_f16 v[98:113], v[198:201], v[236:239], v[98:113]
	v_mfma_f32_32x32x16_f16 v[82:97], v[220:223], v[232:235], v[82:97]
	v_mfma_f32_32x32x16_f16 v[66:81], v[220:223], v[236:239], v[66:81]
	v_mfma_f32_32x32x16_f16 v[50:65], v[224:227], v[232:235], v[50:65]
	v_mfma_f32_32x32x16_f16 v[34:49], v[224:227], v[236:239], v[34:49]
	v_mfma_f32_32x32x16_f16 v[18:33], v[228:231], v[232:235], v[18:33]
	v_mfma_f32_32x32x16_f16 v[2:17], v[228:231], v[236:239], v[2:17]
	s_waitcnt lgkmcnt(0)
	s_barrier
	s_waitcnt lgkmcnt(1)
	v_mfma_f32_32x32x16_f16 v[114:129], v[154:157], v[170:173], v[114:129]
	s_waitcnt lgkmcnt(0)
	v_mfma_f32_32x32x16_f16 v[98:113], v[154:157], v[174:177], v[98:113]
	ds_read_b128 v[154:157], v215 offset:49152
	ds_read_b128 v[178:181], v215 offset:51200
	ds_read_b128 v[182:185], v215 offset:53248
	ds_read_b128 v[186:189], v215 offset:55296
	ds_read_b128 v[190:193], v214 offset:40960
	ds_read_b128 v[194:197], v214 offset:43008
	s_waitcnt vmcnt(4)
	v_cvt_pk_f16_f32 v150, v150, v151
	v_cvt_pk_f16_f32 v151, v152, v153
	v_cvt_pk_f16_f32 v152, v142, v143
	v_cvt_pk_f16_f32 v153, v144, v145
	ds_write_b64 v209, v[150:151]
	ds_write_b64 v248, v[152:153]
	v_mfma_f32_32x32x16_f16 v[82:97], v[158:161], v[170:173], v[82:97]
	s_waitcnt vmcnt(3)
	ds_write_b128 v208, v[138:141] offset:8192
	s_waitcnt vmcnt(2)
	ds_write_b128 v208, v[146:149] offset:16384
	v_mfma_f32_32x32x16_f16 v[66:81], v[158:161], v[174:177], v[66:81]
	v_mfma_f32_32x32x16_f16 v[50:65], v[162:165], v[170:173], v[50:65]
	s_waitcnt vmcnt(1)
	ds_write_b128 v208, v[134:137] offset:24576
	s_waitcnt vmcnt(0)
	ds_write_b128 v208, v[130:133] offset:32768
	v_mfma_f32_32x32x16_f16 v[34:49], v[162:165], v[174:177], v[34:49]
	v_mfma_f32_32x32x16_f16 v[18:33], v[166:169], v[170:173], v[18:33]
	v_mfma_f32_32x32x16_f16 v[2:17], v[166:169], v[174:177], v[2:17]
	v_add_u32_e32 v158, 0x16000, v211
	v_add_u32_e32 v142, v158, v210
	ds_read_b128 v[130:133], v142
	ds_read_b128 v[134:137], v142 offset:2048
	ds_read_b128 v[138:141], v142 offset:4096
	ds_read_b128 v[142:145], v142 offset:6144
	v_add_u32_e32 v166, 0x14000, v218
	v_add_u32_e32 v150, v166, v210
	ds_read_b128 v[146:149], v150
	ds_read_b128 v[150:153], v150 offset:2048
	s_waitcnt lgkmcnt(12)
	v_mfma_f32_32x32x16_f16 v[114:129], v[154:157], v[190:193], v[114:129]
	s_waitcnt lgkmcnt(11)
	v_mfma_f32_32x32x16_f16 v[98:113], v[154:157], v[194:197], v[98:113]
	v_mfma_f32_32x32x16_f16 v[82:97], v[178:181], v[190:193], v[82:97]
	v_mfma_f32_32x32x16_f16 v[66:81], v[178:181], v[194:197], v[66:81]
	v_mfma_f32_32x32x16_f16 v[50:65], v[182:185], v[190:193], v[50:65]
	v_mfma_f32_32x32x16_f16 v[34:49], v[182:185], v[194:197], v[34:49]
	v_mfma_f32_32x32x16_f16 v[18:33], v[186:189], v[190:193], v[18:33]
	v_mfma_f32_32x32x16_f16 v[2:17], v[186:189], v[194:197], v[2:17]
	s_waitcnt lgkmcnt(0)
	s_barrier
	s_waitcnt lgkmcnt(1)
	v_mfma_f32_32x32x16_f16 v[114:129], v[130:133], v[146:149], v[114:129]
	s_waitcnt lgkmcnt(0)
	v_mfma_f32_32x32x16_f16 v[98:113], v[130:133], v[150:153], v[98:113]
	v_add_u32_e32 v162, v158, v212
	ds_read_b128 v[130:133], v162
	ds_read_b128 v[154:157], v162 offset:2048
	ds_read_b128 v[158:161], v162 offset:4096
	ds_read_b128 v[162:165], v162 offset:6144
	v_add_u32_e32 v170, v166, v212
	ds_read_b128 v[166:169], v170
	ds_read_b128 v[170:173], v170 offset:2048
	v_mfma_f32_32x32x16_f16 v[82:97], v[134:137], v[146:149], v[82:97]
	v_mfma_f32_32x32x16_f16 v[66:81], v[134:137], v[150:153], v[66:81]
	v_mfma_f32_32x32x16_f16 v[50:65], v[138:141], v[146:149], v[50:65]
	v_mfma_f32_32x32x16_f16 v[34:49], v[138:141], v[150:153], v[34:49]
	v_mfma_f32_32x32x16_f16 v[18:33], v[142:145], v[146:149], v[18:33]
	v_mfma_f32_32x32x16_f16 v[2:17], v[142:145], v[150:153], v[2:17]
	ds_read_b128 v[134:137], v216 offset:8192
	ds_read_b128 v[138:141], v216 offset:10240
	ds_read_b128 v[142:145], v216 offset:12288
	ds_read_b128 v[146:149], v216 offset:14336
	ds_read_b128 v[150:153], v217
	ds_read_b128 v[174:177], v217 offset:2048
	s_waitcnt lgkmcnt(7)
	v_mfma_f32_32x32x16_f16 v[114:129], v[130:133], v[166:169], v[114:129]
	s_waitcnt lgkmcnt(6)
	v_mfma_f32_32x32x16_f16 v[98:113], v[130:133], v[170:173], v[98:113]
	v_mfma_f32_32x32x16_f16 v[82:97], v[154:157], v[166:169], v[82:97]
	v_mfma_f32_32x32x16_f16 v[66:81], v[154:157], v[170:173], v[66:81]
	v_mfma_f32_32x32x16_f16 v[50:65], v[158:161], v[166:169], v[50:65]
	v_mfma_f32_32x32x16_f16 v[34:49], v[158:161], v[170:173], v[34:49]
	v_mfma_f32_32x32x16_f16 v[18:33], v[162:165], v[166:169], v[18:33]
	v_mfma_f32_32x32x16_f16 v[2:17], v[162:165], v[170:173], v[2:17]
	s_waitcnt lgkmcnt(0)
	s_barrier
	s_waitcnt lgkmcnt(1)
	v_mfma_f32_32x32x16_f16 v[114:129], v[134:137], v[150:153], v[114:129]
	s_waitcnt lgkmcnt(0)
	v_mfma_f32_32x32x16_f16 v[98:113], v[134:137], v[174:177], v[98:113]
	ds_read_b128 v[130:133], v215 offset:8192
	ds_read_b128 v[134:137], v215 offset:10240
	ds_read_b128 v[154:157], v215 offset:12288
	ds_read_b128 v[158:161], v215 offset:14336
	ds_read_b128 v[162:165], v214
	ds_read_b128 v[166:169], v214 offset:2048
	v_mfma_f32_32x32x16_f16 v[82:97], v[138:141], v[150:153], v[82:97]
	v_mfma_f32_32x32x16_f16 v[66:81], v[138:141], v[174:177], v[66:81]
	v_mfma_f32_32x32x16_f16 v[50:65], v[142:145], v[150:153], v[50:65]
	v_mfma_f32_32x32x16_f16 v[34:49], v[142:145], v[174:177], v[34:49]
	v_mfma_f32_32x32x16_f16 v[18:33], v[146:149], v[150:153], v[18:33]
	v_mfma_f32_32x32x16_f16 v[2:17], v[146:149], v[174:177], v[2:17]
	s_waitcnt lgkmcnt(1)
	v_mfma_f32_32x32x16_f16 v[114:129], v[130:133], v[162:165], v[114:129]
	s_waitcnt lgkmcnt(0)
	v_mfma_f32_32x32x16_f16 v[98:113], v[130:133], v[166:169], v[98:113]
	v_mfma_f32_32x32x16_f16 v[82:97], v[134:137], v[162:165], v[82:97]
	v_mfma_f32_32x32x16_f16 v[66:81], v[134:137], v[166:169], v[66:81]
	v_mfma_f32_32x32x16_f16 v[50:65], v[154:157], v[162:165], v[50:65]
	v_mfma_f32_32x32x16_f16 v[34:49], v[154:157], v[166:169], v[34:49]
	v_mfma_f32_32x32x16_f16 v[18:33], v[158:161], v[162:165], v[18:33]
	v_mfma_f32_32x32x16_f16 v[2:17], v[158:161], v[166:169], v[2:17]
	v_lshl_or_b32 v130, v207, 2, s31
	s_waitcnt lgkmcnt(0)
	s_barrier
	v_lshlrev_b32_e32 v154, 2, v130
	global_load_dwordx4 v[134:137], v154, s[0:1]
	global_load_dwordx4 v[150:153], v154, s[0:1] offset:32
	global_load_dwordx4 v[156:159], v154, s[0:1] offset:64
	global_load_dwordx4 v[160:163], v154, s[0:1] offset:96
	global_load_dwordx4 v[164:167], v154, s[0:1] offset:128
	global_load_dwordx4 v[168:171], v154, s[0:1] offset:160
	s_movk_i32 s4, 0x410
	v_lshlrev_b32_e32 v130, 1, v130
	v_mul_lo_u32 v131, v206, s4
	v_add3_u32 v155, 0, v130, v131
	global_load_dwordx4 v[172:175], v154, s[0:1] offset:192
	global_load_dwordx4 v[146:149], v154, s[0:1] offset:224
	global_load_dwordx4 v[142:145], v154, s[0:1] offset:256
	global_load_dwordx4 v[130:133], v154, s[0:1] offset:288
	global_load_dwordx4 v[138:141], v154, s[0:1] offset:320
	v_add_u32_e32 v176, 0x8000, v155
	s_waitcnt vmcnt(10)
	v_pk_add_f32 v[114:115], v[134:135], v[114:115]
	v_pk_add_f32 v[116:117], v[136:137], v[116:117]
	v_pk_add_f32 v[98:99], v[134:135], v[98:99]
	v_pk_add_f32 v[100:101], v[136:137], v[100:101]
	s_waitcnt vmcnt(9)
	v_pk_add_f32 v[118:119], v[150:151], v[118:119]
	v_pk_add_f32 v[120:121], v[152:153], v[120:121]
	s_waitcnt vmcnt(6)
	v_pk_add_f32 v[82:83], v[164:165], v[82:83]
	v_pk_add_f32 v[84:85], v[166:167], v[84:85]
	v_pk_add_f32 v[66:67], v[164:165], v[66:67]
	v_pk_add_f32 v[68:69], v[166:167], v[68:69]
	s_waitcnt vmcnt(5)
	v_pk_add_f32 v[70:71], v[168:169], v[70:71]
	v_pk_add_f32 v[72:73], v[170:171], v[72:73]
	v_pk_add_f32 v[102:103], v[150:151], v[102:103]
	v_pk_add_f32 v[104:105], v[152:153], v[104:105]
	v_pk_add_f32 v[122:123], v[156:157], v[122:123]
	v_pk_add_f32 v[124:125], v[158:159], v[124:125]
	v_pk_add_f32 v[106:107], v[156:157], v[106:107]
	v_pk_add_f32 v[108:109], v[158:159], v[108:109]
	v_pk_add_f32 v[126:127], v[160:161], v[126:127]
	v_pk_add_f32 v[128:129], v[162:163], v[128:129]
	v_pk_add_f32 v[110:111], v[160:161], v[110:111]
	v_pk_add_f32 v[112:113], v[162:163], v[112:113]
	v_pk_add_f32 v[86:87], v[168:169], v[86:87]
	v_pk_mul_f32 v[114:115], v[202:203], v[114:115] op_sel_hi:[0,1]
	v_pk_mul_f32 v[116:117], v[202:203], v[116:117] op_sel_hi:[0,1]
	v_pk_mul_f32 v[98:99], v[202:203], v[98:99] op_sel_hi:[0,1]
	v_pk_mul_f32 v[100:101], v[202:203], v[100:101] op_sel_hi:[0,1]
	v_pk_mul_f32 v[118:119], v[202:203], v[118:119] op_sel_hi:[0,1]
	v_pk_mul_f32 v[120:121], v[202:203], v[120:121] op_sel_hi:[0,1]
	v_pk_mul_f32 v[82:83], v[202:203], v[82:83] op_sel_hi:[0,1]
	v_pk_mul_f32 v[84:85], v[202:203], v[84:85] op_sel_hi:[0,1]
	v_pk_mul_f32 v[66:67], v[202:203], v[66:67] op_sel_hi:[0,1]
	v_pk_mul_f32 v[68:69], v[202:203], v[68:69] op_sel_hi:[0,1]
	v_pk_add_f32 v[88:89], v[170:171], v[88:89]
	v_pk_mul_f32 v[70:71], v[202:203], v[70:71] op_sel_hi:[0,1]
	v_pk_mul_f32 v[72:73], v[202:203], v[72:73] op_sel_hi:[0,1]
	v_pk_mul_f32 v[102:103], v[202:203], v[102:103] op_sel_hi:[0,1]
	v_pk_mul_f32 v[104:105], v[202:203], v[104:105] op_sel_hi:[0,1]
	v_pk_mul_f32 v[122:123], v[202:203], v[122:123] op_sel_hi:[0,1]
	v_pk_mul_f32 v[124:125], v[202:203], v[124:125] op_sel_hi:[0,1]
	v_pk_mul_f32 v[106:107], v[202:203], v[106:107] op_sel_hi:[0,1]
	v_pk_mul_f32 v[108:109], v[202:203], v[108:109] op_sel_hi:[0,1]
	v_pk_mul_f32 v[126:127], v[202:203], v[126:127] op_sel_hi:[0,1]
	v_pk_mul_f32 v[128:129], v[202:203], v[128:129] op_sel_hi:[0,1]
	v_pk_mul_f32 v[110:111], v[202:203], v[110:111] op_sel_hi:[0,1]
	v_pk_mul_f32 v[112:113], v[202:203], v[112:113] op_sel_hi:[0,1]
	v_pk_mul_f32 v[86:87], v[202:203], v[86:87] op_sel_hi:[0,1]
	v_cvt_pk_f16_f32 v114, v114, v115
	v_cvt_pk_f16_f32 v115, v116, v117
	v_cvt_pk_f16_f32 v98, v98, v99
	v_cvt_pk_f16_f32 v99, v100, v101
	v_cvt_pk_f16_f32 v100, v118, v119
	v_cvt_pk_f16_f32 v101, v120, v121
	v_cvt_pk_f16_f32 v82, v82, v83
	v_cvt_pk_f16_f32 v83, v84, v85
	v_cvt_pk_f16_f32 v84, v66, v67
	v_cvt_pk_f16_f32 v85, v68, v69
	v_pk_mul_f32 v[88:89], v[202:203], v[88:89] op_sel_hi:[0,1]
	v_cvt_pk_f16_f32 v70, v70, v71
	v_cvt_pk_f16_f32 v71, v72, v73
	v_cvt_pk_f16_f32 v102, v102, v103
	v_cvt_pk_f16_f32 v103, v104, v105
	v_cvt_pk_f16_f32 v104, v122, v123
	v_cvt_pk_f16_f32 v105, v124, v125
	v_cvt_pk_f16_f32 v106, v106, v107
	v_cvt_pk_f16_f32 v107, v108, v109
	v_cvt_pk_f16_f32 v108, v126, v127
	v_cvt_pk_f16_f32 v109, v128, v129
	v_cvt_pk_f16_f32 v110, v110, v111
	v_cvt_pk_f16_f32 v111, v112, v113
	v_cvt_pk_f16_f32 v86, v86, v87
	ds_write2_b64 v155, v[114:115], v[100:101] offset1:2
	ds_write2_b64 v176, v[98:99], v[102:103] offset0:64 offset1:66
	ds_write2_b64 v155, v[104:105], v[108:109] offset0:4 offset1:6
	ds_write2_b64 v176, v[106:107], v[110:111] offset0:68 offset1:70
	v_cvt_pk_f16_f32 v87, v88, v89
	ds_write2_b64 v176, v[84:85], v[70:71] offset0:72 offset1:74
	s_waitcnt vmcnt(4)
	v_pk_add_f32 v[70:71], v[172:173], v[90:91]
	v_pk_add_f32 v[84:85], v[174:175], v[92:93]
	v_pk_add_f32 v[74:75], v[172:173], v[74:75]
	ds_write2_b64 v155, v[82:83], v[86:87] offset0:8 offset1:10
	v_pk_mul_f32 v[82:83], v[202:203], v[70:71] op_sel_hi:[0,1]
	v_pk_mul_f32 v[84:85], v[202:203], v[84:85] op_sel_hi:[0,1]
	v_pk_mul_f32 v[74:75], v[202:203], v[74:75] op_sel_hi:[0,1]
	global_load_dwordx4 v[66:69], v154, s[0:1] offset:352
	global_load_dwordx4 v[70:73], v154, s[0:1] offset:384
	v_cvt_pk_f16_f32 v82, v82, v83
	v_cvt_pk_f16_f32 v83, v84, v85
	v_cvt_pk_f16_f32 v84, v74, v75
	v_pk_add_f32 v[74:75], v[174:175], v[76:77]
	s_waitcnt vmcnt(5)
	v_pk_add_f32 v[78:79], v[146:147], v[78:79]
	v_pk_mul_f32 v[74:75], v[202:203], v[74:75] op_sel_hi:[0,1]
	v_cvt_pk_f16_f32 v85, v74, v75
	global_load_dwordx4 v[74:77], v154, s[0:1] offset:416
	v_pk_add_f32 v[80:81], v[148:149], v[80:81]
	v_pk_mul_f32 v[78:79], v[202:203], v[78:79] op_sel_hi:[0,1]
	v_pk_mul_f32 v[80:81], v[202:203], v[80:81] op_sel_hi:[0,1]
	v_cvt_pk_f16_f32 v78, v78, v79
	v_cvt_pk_f16_f32 v79, v80, v81
	ds_write2_b64 v176, v[84:85], v[78:79] offset0:76 offset1:78
	global_load_dwordx4 v[78:81], v154, s[0:1] offset:448
	v_pk_add_f32 v[86:87], v[146:147], v[94:95]
	v_pk_add_f32 v[88:89], v[148:149], v[96:97]
	s_waitcnt vmcnt(6)
	v_pk_add_f32 v[50:51], v[142:143], v[50:51]
	v_pk_add_f32 v[52:53], v[144:145], v[52:53]
	v_pk_add_f32 v[34:35], v[142:143], v[34:35]
	v_pk_mul_f32 v[86:87], v[202:203], v[86:87] op_sel_hi:[0,1]
	v_pk_mul_f32 v[88:89], v[202:203], v[88:89] op_sel_hi:[0,1]
	v_pk_mul_f32 v[50:51], v[202:203], v[50:51] op_sel_hi:[0,1]
	v_pk_mul_f32 v[52:53], v[202:203], v[52:53] op_sel_hi:[0,1]
	v_pk_mul_f32 v[34:35], v[202:203], v[34:35] op_sel_hi:[0,1]
	v_cvt_pk_f16_f32 v86, v86, v87
	v_cvt_pk_f16_f32 v87, v88, v89
	v_cvt_pk_f16_f32 v50, v50, v51
	v_cvt_pk_f16_f32 v51, v52, v53
	v_cvt_pk_f16_f32 v52, v34, v35
	v_pk_add_f32 v[34:35], v[144:145], v[36:37]
	ds_write2_b64 v155, v[82:83], v[86:87] offset0:12 offset1:14
	v_pk_mul_f32 v[82:83], v[202:203], v[34:35] op_sel_hi:[0,1]
	global_load_dwordx4 v[34:37], v154, s[0:1] offset:480
	s_waitcnt vmcnt(6)
	v_pk_add_f32 v[38:39], v[130:131], v[38:39]
	v_pk_add_f32 v[40:41], v[132:133], v[40:41]
	v_pk_mul_f32 v[38:39], v[202:203], v[38:39] op_sel_hi:[0,1]
	v_pk_mul_f32 v[40:41], v[202:203], v[40:41] op_sel_hi:[0,1]
	v_cvt_pk_f16_f32 v53, v82, v83
	v_cvt_pk_f16_f32 v38, v38, v39
	v_cvt_pk_f16_f32 v39, v40, v41
	ds_write2_b64 v176, v[52:53], v[38:39] offset0:80 offset1:82
	s_waitcnt vmcnt(5)
	v_pk_add_f32 v[38:39], v[138:139], v[58:59]
	v_pk_add_f32 v[40:41], v[140:141], v[60:61]
	v_pk_mul_f32 v[38:39], v[202:203], v[38:39] op_sel_hi:[0,1]
	v_pk_mul_f32 v[40:41], v[202:203], v[40:41] op_sel_hi:[0,1]
	v_cvt_pk_f16_f32 v38, v38, v39
	v_cvt_pk_f16_f32 v39, v40, v41
	v_pk_add_f32 v[40:41], v[138:139], v[42:43]
	v_pk_add_f32 v[42:43], v[140:141], v[44:45]
	v_pk_mul_f32 v[40:41], v[202:203], v[40:41] op_sel_hi:[0,1]
	v_pk_mul_f32 v[42:43], v[202:203], v[42:43] op_sel_hi:[0,1]
	v_cvt_pk_f16_f32 v40, v40, v41
	v_cvt_pk_f16_f32 v41, v42, v43
	v_pk_add_f32 v[54:55], v[130:131], v[54:55]
	v_pk_add_f32 v[56:57], v[132:133], v[56:57]
	v_pk_mul_f32 v[54:55], v[202:203], v[54:55] op_sel_hi:[0,1]
	v_pk_mul_f32 v[56:57], v[202:203], v[56:57] op_sel_hi:[0,1]
	v_cmp_gt_u32_e64 s[0:1], 8, v0
	v_cvt_pk_f16_f32 v54, v54, v55
	v_cvt_pk_f16_f32 v55, v56, v57
	s_and_b64 s[6:7], s[20:21], s[0:1]
	ds_write2_b64 v155, v[50:51], v[54:55] offset0:16 offset1:18
	s_waitcnt vmcnt(4)
	v_pk_add_f32 v[42:43], v[66:67], v[62:63]
	s_waitcnt vmcnt(3)
	v_pk_add_f32 v[18:19], v[70:71], v[18:19]
	v_pk_add_f32 v[20:21], v[72:73], v[20:21]
	v_pk_add_f32 v[2:3], v[70:71], v[2:3]
	v_pk_add_f32 v[4:5], v[72:73], v[4:5]
	v_pk_mul_f32 v[18:19], v[202:203], v[18:19] op_sel_hi:[0,1]
	v_pk_mul_f32 v[20:21], v[202:203], v[20:21] op_sel_hi:[0,1]
	v_pk_mul_f32 v[2:3], v[202:203], v[2:3] op_sel_hi:[0,1]
	v_pk_mul_f32 v[4:5], v[202:203], v[4:5] op_sel_hi:[0,1]
	v_cvt_pk_f16_f32 v18, v18, v19
	v_cvt_pk_f16_f32 v19, v20, v21
	v_cvt_pk_f16_f32 v2, v2, v3
	v_cvt_pk_f16_f32 v3, v4, v5
	s_waitcnt vmcnt(2)
	v_pk_add_f32 v[4:5], v[74:75], v[22:23]
	v_pk_add_f32 v[20:21], v[76:77], v[24:25]
	v_pk_mul_f32 v[4:5], v[202:203], v[4:5] op_sel_hi:[0,1]
	v_pk_mul_f32 v[20:21], v[202:203], v[20:21] op_sel_hi:[0,1]
	v_cvt_pk_f16_f32 v4, v4, v5
	v_cvt_pk_f16_f32 v5, v20, v21
	ds_write2_b64 v155, v[18:19], v[4:5] offset0:24 offset1:26
	v_pk_add_f32 v[4:5], v[74:75], v[6:7]
	v_pk_add_f32 v[6:7], v[76:77], v[8:9]
	v_pk_mul_f32 v[4:5], v[202:203], v[4:5] op_sel_hi:[0,1]
	v_pk_mul_f32 v[6:7], v[202:203], v[6:7] op_sel_hi:[0,1]
	v_cvt_pk_f16_f32 v4, v4, v5
	v_cvt_pk_f16_f32 v5, v6, v7
	ds_write2_b64 v176, v[2:3], v[4:5] offset0:88 offset1:90
	s_waitcnt vmcnt(1)
	v_pk_add_f32 v[2:3], v[78:79], v[26:27]
	v_pk_add_f32 v[4:5], v[80:81], v[28:29]
	v_pk_mul_f32 v[2:3], v[202:203], v[2:3] op_sel_hi:[0,1]
	v_pk_mul_f32 v[4:5], v[202:203], v[4:5] op_sel_hi:[0,1]
	v_cvt_pk_f16_f32 v2, v2, v3
	v_cvt_pk_f16_f32 v3, v4, v5
	v_pk_add_f32 v[4:5], v[78:79], v[10:11]
	v_pk_add_f32 v[6:7], v[80:81], v[12:13]
	v_pk_mul_f32 v[4:5], v[202:203], v[4:5] op_sel_hi:[0,1]
	v_pk_mul_f32 v[6:7], v[202:203], v[6:7] op_sel_hi:[0,1]
	v_pk_add_f32 v[44:45], v[68:69], v[64:65]
	v_cvt_pk_f16_f32 v4, v4, v5
	v_cvt_pk_f16_f32 v5, v6, v7
	s_waitcnt vmcnt(0)
	v_pk_add_f32 v[6:7], v[34:35], v[30:31]
	v_pk_add_f32 v[8:9], v[36:37], v[32:33]
	v_pk_mul_f32 v[42:43], v[202:203], v[42:43] op_sel_hi:[0,1]
	v_pk_mul_f32 v[44:45], v[202:203], v[44:45] op_sel_hi:[0,1]
	v_pk_mul_f32 v[6:7], v[202:203], v[6:7] op_sel_hi:[0,1]
	v_pk_mul_f32 v[8:9], v[202:203], v[8:9] op_sel_hi:[0,1]
	v_cvt_pk_f16_f32 v42, v42, v43
	v_cvt_pk_f16_f32 v43, v44, v45
	v_cvt_pk_f16_f32 v6, v6, v7
	v_cvt_pk_f16_f32 v7, v8, v9
	ds_write2_b64 v155, v[38:39], v[42:43] offset0:20 offset1:22
	v_pk_add_f32 v[38:39], v[66:67], v[46:47]
	v_pk_add_f32 v[42:43], v[68:69], v[48:49]
	ds_write2_b64 v155, v[2:3], v[6:7] offset0:28 offset1:30
	v_pk_add_f32 v[2:3], v[34:35], v[14:15]
	v_pk_add_f32 v[6:7], v[36:37], v[16:17]
	v_pk_mul_f32 v[38:39], v[202:203], v[38:39] op_sel_hi:[0,1]
	v_pk_mul_f32 v[42:43], v[202:203], v[42:43] op_sel_hi:[0,1]
	v_pk_mul_f32 v[2:3], v[202:203], v[2:3] op_sel_hi:[0,1]
	v_pk_mul_f32 v[6:7], v[202:203], v[6:7] op_sel_hi:[0,1]
	v_cvt_pk_f16_f32 v38, v38, v39
	v_cvt_pk_f16_f32 v39, v42, v43
	v_cvt_pk_f16_f32 v2, v2, v3
	v_cvt_pk_f16_f32 v3, v6, v7
	ds_write2_b64 v176, v[40:41], v[38:39] offset0:84 offset1:86
	ds_write2_b64 v176, v[4:5], v[2:3] offset0:92 offset1:94
	s_and_saveexec_b64 s[4:5], s[6:7]
	v_lshl_add_u32 v2, v0, 2, 0
	v_add_u32_e32 v2, 0x20800, v2
	v_mov_b32_e32 v3, 0
	ds_write_b32 v2, v3
	s_or_b64 exec, exec, s[4:5]
	s_waitcnt lgkmcnt(0)
	s_barrier
	s_mov_b64 s[4:5], -1
	s_and_b64 vcc, exec, s[22:23]
	s_cbranch_vccnz .LBB1_7
	s_andn2_b64 vcc, exec, s[4:5]
	s_cbranch_vccz .LBB1_14
